# v43 + spatial gating unit: the four transposed LDS reads of each k-step issued together with counted waits (extra temp quads) instead of read-wait-mfma x4
# speedup vs baseline: 1.0127x; 1.0078x over previous
; #define LAS __attribute__((address_space(3)))
; __device__ __forceinline__ void sgu_unit(LAS unsigned char* lds, int unit, const bf16* U, const bf16* VG, const bf16* Wsb, const float* bs, const float* lng, const float* lnb, bf16* YA, const float* stat, int tid_in, int lane_in, int wave, unsigned* probe_words = nullptr) {
;     ...
;             for (int kk = 0; kk < 4; ++kk) if (kk <= (wave >> 1)) {
; #pragma unroll
;                 for (int nn = 0; nn < 4; ++nn) { const LAS unsigned char* ap = tb + kk * (32 * 512) + (((gi * 8 + nn * 2) ^ xkp) * 16);
;                     const s16x4s lo = __builtin_bit_cast(s16x4s, __builtin_amdgcn_ds_read_tr16_b64_v4i16((LAS s16x4s*)ap)), hi = __builtin_bit_cast(s16x4s, __builtin_amdgcn_ds_read_tr16_b64_v4i16((LAS s16x4s*)(ap + 4 * 512)));
;                     const bf16x8 vf = {lo[0], lo[1], lo[2], lo[3], hi[0], hi[1], hi[2], hi[3]};
;                     acc[nn] = __builtin_amdgcn_mfma_f32_16x16x32_bf16(vf, wf[gi][kk], acc[nn], 0, 0, 0); }
;             }
.LBB0_997:
	ds_read_b64_tr_b16 v[56:57], v124 offset:53248
	ds_read_b64_tr_b16 v[58:59], v124 offset:55296
	ds_read_b64_tr_b16 v[144:145], v123 offset:53248
	ds_read_b64_tr_b16 v[146:147], v123 offset:55296
	ds_read_b64_tr_b16 v[148:149], v122 offset:53248
	ds_read_b64_tr_b16 v[150:151], v122 offset:55296
	ds_read_b64_tr_b16 v[152:153], v2 offset:53248
	ds_read_b64_tr_b16 v[154:155], v2 offset:55296
	s_waitcnt lgkmcnt(6)
	v_mfma_f32_16x16x32_bf16 v[76:79], v[56:59], v[52:55], v[76:79]
	s_waitcnt lgkmcnt(4)
	v_mfma_f32_16x16x32_bf16 v[72:75], v[144:147], v[52:55], v[72:75]
	s_waitcnt lgkmcnt(2)
	v_mfma_f32_16x16x32_bf16 v[68:71], v[148:151], v[52:55], v[68:71]
	s_waitcnt lgkmcnt(0)
	v_mfma_f32_16x16x32_bf16 v[80:83], v[152:155], v[52:55], v[80:83]

; #define LAS __attribute__((address_space(3)))
; __device__ __forceinline__ void sgu_unit(LAS unsigned char* lds, int unit, const bf16* U, const bf16* VG, const bf16* Wsb, const float* bs, const float* lng, const float* lnb, bf16* YA, const float* stat, int tid_in, int lane_in, int wave, unsigned* probe_words = nullptr) {
;     ...
;             for (int kk = 0; kk < 4; ++kk) if (kk <= (wave >> 1)) {
; #pragma unroll
;                 for (int nn = 0; nn < 4; ++nn) { const LAS unsigned char* ap = tb + kk * (32 * 512) + (((gi * 8 + nn * 2) ^ xkp) * 16);
;                     const s16x4s lo = __builtin_bit_cast(s16x4s, __builtin_amdgcn_ds_read_tr16_b64_v4i16((LAS s16x4s*)ap)), hi = __builtin_bit_cast(s16x4s, __builtin_amdgcn_ds_read_tr16_b64_v4i16((LAS s16x4s*)(ap + 4 * 512)));
;                     const bf16x8 vf = {lo[0], lo[1], lo[2], lo[3], hi[0], hi[1], hi[2], hi[3]};
;                     acc[nn] = __builtin_amdgcn_mfma_f32_16x16x32_bf16(vf, wf[gi][kk], acc[nn], 0, 0, 0); }
;             }
.LBB0_1002:
	ds_read_b64_tr_b16 v[40:41], v75 offset:53248
	ds_read_b64_tr_b16 v[42:43], v75 offset:55296
	ds_read_b64_tr_b16 v[144:145], v74 offset:53248
	ds_read_b64_tr_b16 v[146:147], v74 offset:55296
	ds_read_b64_tr_b16 v[148:149], v73 offset:53248
	ds_read_b64_tr_b16 v[150:151], v73 offset:55296
	ds_read_b64_tr_b16 v[152:153], v72 offset:53248
	ds_read_b64_tr_b16 v[154:155], v72 offset:55296
	s_waitcnt lgkmcnt(6)
	v_mfma_f32_16x16x32_bf16 v[60:63], v[40:43], v[36:39], v[60:63]
	s_waitcnt lgkmcnt(4)
	v_mfma_f32_16x16x32_bf16 v[56:59], v[144:147], v[36:39], v[56:59]
	s_waitcnt lgkmcnt(2)
	v_mfma_f32_16x16x32_bf16 v[52:55], v[148:151], v[36:39], v[52:55]
	s_waitcnt lgkmcnt(0)
	v_mfma_f32_16x16x32_bf16 v[64:67], v[152:155], v[36:39], v[64:67]

; #define LAS __attribute__((address_space(3)))
; __device__ __forceinline__ void sgu_unit(LAS unsigned char* lds, int unit, const bf16* U, const bf16* VG, const bf16* Wsb, const float* bs, const float* lng, const float* lnb, bf16* YA, const float* stat, int tid_in, int lane_in, int wave, unsigned* probe_words = nullptr) {
;     ...
;             for (int kk = 0; kk < 4; ++kk) if (kk <= (wave >> 1)) {
; #pragma unroll
;                 for (int nn = 0; nn < 4; ++nn) { const LAS unsigned char* ap = tb + kk * (32 * 512) + (((gi * 8 + nn * 2) ^ xkp) * 16);
;                     const s16x4s lo = __builtin_bit_cast(s16x4s, __builtin_amdgcn_ds_read_tr16_b64_v4i16((LAS s16x4s*)ap)), hi = __builtin_bit_cast(s16x4s, __builtin_amdgcn_ds_read_tr16_b64_v4i16((LAS s16x4s*)(ap + 4 * 512)));
;                     const bf16x8 vf = {lo[0], lo[1], lo[2], lo[3], hi[0], hi[1], hi[2], hi[3]};
;                     acc[nn] = __builtin_amdgcn_mfma_f32_16x16x32_bf16(vf, wf[gi][kk], acc[nn], 0, 0, 0); }
;             }
.LBB0_1007:
	ds_read_b64_tr_b16 v[24:25], v124 offset:53504
	ds_read_b64_tr_b16 v[26:27], v124 offset:55552
	ds_read_b64_tr_b16 v[144:145], v123 offset:53504
	ds_read_b64_tr_b16 v[146:147], v123 offset:55552
	ds_read_b64_tr_b16 v[148:149], v122 offset:53504
	ds_read_b64_tr_b16 v[150:151], v122 offset:55552
	ds_read_b64_tr_b16 v[152:153], v2 offset:53504
	ds_read_b64_tr_b16 v[154:155], v2 offset:55552
	s_waitcnt lgkmcnt(6)
	v_mfma_f32_16x16x32_bf16 v[44:47], v[24:27], v[20:23], v[44:47]
	s_waitcnt lgkmcnt(4)
	v_mfma_f32_16x16x32_bf16 v[40:43], v[144:147], v[20:23], v[40:43]
	s_waitcnt lgkmcnt(2)
	v_mfma_f32_16x16x32_bf16 v[36:39], v[148:151], v[20:23], v[36:39]
	s_waitcnt lgkmcnt(0)
	v_mfma_f32_16x16x32_bf16 v[48:51], v[152:155], v[20:23], v[48:51]

; #define LAS __attribute__((address_space(3)))
; __device__ __forceinline__ void sgu_unit(LAS unsigned char* lds, int unit, const bf16* U, const bf16* VG, const bf16* Wsb, const float* bs, const float* lng, const float* lnb, bf16* YA, const float* stat, int tid_in, int lane_in, int wave, unsigned* probe_words = nullptr) {
;     ...
;             for (int kk = 0; kk < 4; ++kk) if (kk <= (wave >> 1)) {
; #pragma unroll
;                 for (int nn = 0; nn < 4; ++nn) { const LAS unsigned char* ap = tb + kk * (32 * 512) + (((gi * 8 + nn * 2) ^ xkp) * 16);
;                     const s16x4s lo = __builtin_bit_cast(s16x4s, __builtin_amdgcn_ds_read_tr16_b64_v4i16((LAS s16x4s*)ap)), hi = __builtin_bit_cast(s16x4s, __builtin_amdgcn_ds_read_tr16_b64_v4i16((LAS s16x4s*)(ap + 4 * 512)));
;                     const bf16x8 vf = {lo[0], lo[1], lo[2], lo[3], hi[0], hi[1], hi[2], hi[3]};
;                     acc[nn] = __builtin_amdgcn_mfma_f32_16x16x32_bf16(vf, wf[gi][kk], acc[nn], 0, 0, 0); }
;             }
.LBB0_1012:
	ds_read_b64_tr_b16 v[8:9], v75 offset:53504
	ds_read_b64_tr_b16 v[10:11], v75 offset:55552
	ds_read_b64_tr_b16 v[144:145], v74 offset:53504
	ds_read_b64_tr_b16 v[146:147], v74 offset:55552
	ds_read_b64_tr_b16 v[148:149], v73 offset:53504
	ds_read_b64_tr_b16 v[150:151], v73 offset:55552
	ds_read_b64_tr_b16 v[152:153], v72 offset:53504
	ds_read_b64_tr_b16 v[154:155], v72 offset:55552
	s_waitcnt lgkmcnt(6)
	v_mfma_f32_16x16x32_bf16 v[28:31], v[8:11], v[4:7], v[28:31]
	s_waitcnt lgkmcnt(4)
	v_mfma_f32_16x16x32_bf16 v[24:27], v[144:147], v[4:7], v[24:27]
	s_waitcnt lgkmcnt(2)
	v_mfma_f32_16x16x32_bf16 v[20:23], v[148:151], v[4:7], v[20:23]
	s_waitcnt lgkmcnt(0)
	v_mfma_f32_16x16x32_bf16 v[32:35], v[152:155], v[4:7], v[32:35]

; #define LAS __attribute__((address_space(3)))
; __device__ __forceinline__ void sgu_unit(LAS unsigned char* lds, int unit, const bf16* U, const bf16* VG, const bf16* Wsb, const float* bs, const float* lng, const float* lnb, bf16* YA, const float* stat, int tid_in, int lane_in, int wave, unsigned* probe_words = nullptr) {
;     ...
;             for (int kk = 0; kk < 4; ++kk) if (kk <= (wave >> 1)) {
; #pragma unroll
;                 for (int nn = 0; nn < 4; ++nn) { const LAS unsigned char* ap = tb + kk * (32 * 512) + (((gi * 8 + nn * 2) ^ xkp) * 16);
;                     const s16x4s lo = __builtin_bit_cast(s16x4s, __builtin_amdgcn_ds_read_tr16_b64_v4i16((LAS s16x4s*)ap)), hi = __builtin_bit_cast(s16x4s, __builtin_amdgcn_ds_read_tr16_b64_v4i16((LAS s16x4s*)(ap + 4 * 512)));
;                     const bf16x8 vf = {lo[0], lo[1], lo[2], lo[3], hi[0], hi[1], hi[2], hi[3]};
;                     acc[nn] = __builtin_amdgcn_mfma_f32_16x16x32_bf16(vf, wf[gi][kk], acc[nn], 0, 0, 0); }
;             }
.LBB0_1018:
	ds_read_b64_tr_b16 v[60:61], v124 offset:36864
	ds_read_b64_tr_b16 v[62:63], v124 offset:38912
	ds_read_b64_tr_b16 v[144:145], v123 offset:36864
	ds_read_b64_tr_b16 v[146:147], v123 offset:38912
	ds_read_b64_tr_b16 v[148:149], v122 offset:36864
	ds_read_b64_tr_b16 v[150:151], v122 offset:38912
	ds_read_b64_tr_b16 v[152:153], v2 offset:36864
	ds_read_b64_tr_b16 v[154:155], v2 offset:38912
	s_waitcnt lgkmcnt(6)
	v_mfma_f32_16x16x32_bf16 v[76:79], v[60:63], v[56:59], v[76:79]
	s_waitcnt lgkmcnt(4)
	v_mfma_f32_16x16x32_bf16 v[72:75], v[144:147], v[56:59], v[72:75]
	s_waitcnt lgkmcnt(2)
	v_mfma_f32_16x16x32_bf16 v[68:71], v[148:151], v[56:59], v[68:71]
	s_waitcnt lgkmcnt(0)
	v_mfma_f32_16x16x32_bf16 v[80:83], v[152:155], v[56:59], v[80:83]
	s_and_b64 vcc, exec, s[4:5]
	s_cbranch_vccz .LBB0_997
	s_branch .LBB0_998

; #define LAS __attribute__((address_space(3)))
; __device__ __forceinline__ void sgu_unit(LAS unsigned char* lds, int unit, const bf16* U, const bf16* VG, const bf16* Wsb, const float* bs, const float* lng, const float* lnb, bf16* YA, const float* stat, int tid_in, int lane_in, int wave, unsigned* probe_words = nullptr) {
;     ...
;             for (int kk = 0; kk < 4; ++kk) if (kk <= (wave >> 1)) {
; #pragma unroll
;                 for (int nn = 0; nn < 4; ++nn) { const LAS unsigned char* ap = tb + kk * (32 * 512) + (((gi * 8 + nn * 2) ^ xkp) * 16);
;                     const s16x4s lo = __builtin_bit_cast(s16x4s, __builtin_amdgcn_ds_read_tr16_b64_v4i16((LAS s16x4s*)ap)), hi = __builtin_bit_cast(s16x4s, __builtin_amdgcn_ds_read_tr16_b64_v4i16((LAS s16x4s*)(ap + 4 * 512)));
;                     const bf16x8 vf = {lo[0], lo[1], lo[2], lo[3], hi[0], hi[1], hi[2], hi[3]};
;                     acc[nn] = __builtin_amdgcn_mfma_f32_16x16x32_bf16(vf, wf[gi][kk], acc[nn], 0, 0, 0); }
;             }
.LBB0_1021:
	ds_read_b64_tr_b16 v[44:45], v75 offset:36864
	ds_read_b64_tr_b16 v[46:47], v75 offset:38912
	ds_read_b64_tr_b16 v[144:145], v74 offset:36864
	ds_read_b64_tr_b16 v[146:147], v74 offset:38912
	ds_read_b64_tr_b16 v[148:149], v73 offset:36864
	ds_read_b64_tr_b16 v[150:151], v73 offset:38912
	ds_read_b64_tr_b16 v[152:153], v72 offset:36864
	ds_read_b64_tr_b16 v[154:155], v72 offset:38912
	s_waitcnt lgkmcnt(6)
	v_mfma_f32_16x16x32_bf16 v[60:63], v[44:47], v[40:43], v[60:63]
	s_waitcnt lgkmcnt(4)
	v_mfma_f32_16x16x32_bf16 v[56:59], v[144:147], v[40:43], v[56:59]
	s_waitcnt lgkmcnt(2)
	v_mfma_f32_16x16x32_bf16 v[52:55], v[148:151], v[40:43], v[52:55]
	s_waitcnt lgkmcnt(0)
	v_mfma_f32_16x16x32_bf16 v[64:67], v[152:155], v[40:43], v[64:67]
	s_and_b64 vcc, exec, s[4:5]
	s_cbranch_vccz .LBB0_1002
	s_branch .LBB0_1003

; #define LAS __attribute__((address_space(3)))
; __device__ __forceinline__ void sgu_unit(LAS unsigned char* lds, int unit, const bf16* U, const bf16* VG, const bf16* Wsb, const float* bs, const float* lng, const float* lnb, bf16* YA, const float* stat, int tid_in, int lane_in, int wave, unsigned* probe_words = nullptr) {
;     ...
;             for (int kk = 0; kk < 4; ++kk) if (kk <= (wave >> 1)) {
; #pragma unroll
;                 for (int nn = 0; nn < 4; ++nn) { const LAS unsigned char* ap = tb + kk * (32 * 512) + (((gi * 8 + nn * 2) ^ xkp) * 16);
;                     const s16x4s lo = __builtin_bit_cast(s16x4s, __builtin_amdgcn_ds_read_tr16_b64_v4i16((LAS s16x4s*)ap)), hi = __builtin_bit_cast(s16x4s, __builtin_amdgcn_ds_read_tr16_b64_v4i16((LAS s16x4s*)(ap + 4 * 512)));
;                     const bf16x8 vf = {lo[0], lo[1], lo[2], lo[3], hi[0], hi[1], hi[2], hi[3]};
;                     acc[nn] = __builtin_amdgcn_mfma_f32_16x16x32_bf16(vf, wf[gi][kk], acc[nn], 0, 0, 0); }
;             }
.LBB0_1024:
	ds_read_b64_tr_b16 v[28:29], v124 offset:37120
	ds_read_b64_tr_b16 v[30:31], v124 offset:39168
	ds_read_b64_tr_b16 v[144:145], v123 offset:37120
	ds_read_b64_tr_b16 v[146:147], v123 offset:39168
	ds_read_b64_tr_b16 v[148:149], v122 offset:37120
	ds_read_b64_tr_b16 v[150:151], v122 offset:39168
	ds_read_b64_tr_b16 v[152:153], v2 offset:37120
	ds_read_b64_tr_b16 v[154:155], v2 offset:39168
	s_waitcnt lgkmcnt(6)
	v_mfma_f32_16x16x32_bf16 v[44:47], v[28:31], v[24:27], v[44:47]
	s_waitcnt lgkmcnt(4)
	v_mfma_f32_16x16x32_bf16 v[40:43], v[144:147], v[24:27], v[40:43]
	s_waitcnt lgkmcnt(2)
	v_mfma_f32_16x16x32_bf16 v[36:39], v[148:151], v[24:27], v[36:39]
	s_waitcnt lgkmcnt(0)
	v_mfma_f32_16x16x32_bf16 v[48:51], v[152:155], v[24:27], v[48:51]
	s_and_b64 vcc, exec, s[4:5]
	s_cbranch_vccz .LBB0_1007
	s_branch .LBB0_1008

; #define LAS __attribute__((address_space(3)))
; __device__ __forceinline__ void sgu_unit(LAS unsigned char* lds, int unit, const bf16* U, const bf16* VG, const bf16* Wsb, const float* bs, const float* lng, const float* lnb, bf16* YA, const float* stat, int tid_in, int lane_in, int wave, unsigned* probe_words = nullptr) {
;     ...
;             for (int kk = 0; kk < 4; ++kk) if (kk <= (wave >> 1)) {
; #pragma unroll
;                 for (int nn = 0; nn < 4; ++nn) { const LAS unsigned char* ap = tb + kk * (32 * 512) + (((gi * 8 + nn * 2) ^ xkp) * 16);
;                     const s16x4s lo = __builtin_bit_cast(s16x4s, __builtin_amdgcn_ds_read_tr16_b64_v4i16((LAS s16x4s*)ap)), hi = __builtin_bit_cast(s16x4s, __builtin_amdgcn_ds_read_tr16_b64_v4i16((LAS s16x4s*)(ap + 4 * 512)));
;                     const bf16x8 vf = {lo[0], lo[1], lo[2], lo[3], hi[0], hi[1], hi[2], hi[3]};
;                     acc[nn] = __builtin_amdgcn_mfma_f32_16x16x32_bf16(vf, wf[gi][kk], acc[nn], 0, 0, 0); }
;             }
.LBB0_1027:
	ds_read_b64_tr_b16 v[12:13], v75 offset:37120
	ds_read_b64_tr_b16 v[14:15], v75 offset:39168
	ds_read_b64_tr_b16 v[144:145], v74 offset:37120
	ds_read_b64_tr_b16 v[146:147], v74 offset:39168
	ds_read_b64_tr_b16 v[148:149], v73 offset:37120
	ds_read_b64_tr_b16 v[150:151], v73 offset:39168
	ds_read_b64_tr_b16 v[152:153], v72 offset:37120
	ds_read_b64_tr_b16 v[154:155], v72 offset:39168
	s_waitcnt lgkmcnt(6)
	v_mfma_f32_16x16x32_bf16 v[28:31], v[12:15], v[8:11], v[28:31]
	s_waitcnt lgkmcnt(4)
	v_mfma_f32_16x16x32_bf16 v[24:27], v[144:147], v[8:11], v[24:27]
	s_waitcnt lgkmcnt(2)
	v_mfma_f32_16x16x32_bf16 v[20:23], v[148:151], v[8:11], v[20:23]
	s_waitcnt lgkmcnt(0)
	v_mfma_f32_16x16x32_bf16 v[32:35], v[152:155], v[8:11], v[32:35]
	s_and_b64 vcc, exec, s[4:5]
	s_cbranch_vccz .LBB0_1012
	s_branch .LBB0_1013
